# baseline (speedup 1.0000x reference)
.Lgru_tile_alt:
	v_mov_b32_e32 v249, 0
	s_cmp_lg_u32 s47, 2
	s_cbranch_scc1 .Lgru_alt_noflag
	v_mov_b32_e32 v249, s54
	global_load_ubyte v249, v249, s[52:53] offset:12 sc0 sc1

.Lgru_restore:
	s_lshl_b32 s58, s54, 17
	s_add_u32 s58, s58, 0x1120000
	s_add_u32 s58, s16, s58
	s_addc_u32 s59, s17, 0
	v_lshlrev_b32_e32 v219, 4, v248
	v_readfirstlane_b32 s55, v248
	s_nop 3
	s_cmp_lg_u32 s55, 0
	s_cbranch_scc1 .Lgru_rs_wait
	s_movk_i32 s56, 0x200
	v_readfirstlane_b32 s57, v249
	s_nop 3
	s_cmp_lg_u32 s57, 0
	s_cbranch_scc1 .Lgru_rs_polled
